# baseline (speedup 1.0000x reference)
.LBB7_5:
	s_add_i32 s10, s11, s8
	s_cmpk_gt_i32 s5, 0x4ff
	s_cselect_b64 s[4:5], -1, 0
	s_and_b64 s[4:5], exec, s[4:5]
	s_mov_b64 vcc, s[4:5]
	s_cbranch_vccz .LBB7_7
	s_lshl_b32 s8, s33, 2
	s_abs_i32 s9, s8
	v_cvt_f32_u32_e32 v1, s9
	s_sub_i32 s13, 0, s9
	s_abs_i32 s11, s10
	s_xor_b32 s12, s10, s8
	v_rcp_iflag_f32_e32 v1, v1
	s_ashr_i32 s12, s12, 31
	v_mul_f32_e32 v1, 0x4f7ffffe, v1
	v_cvt_u32_f32_e32 v1, v1
	s_nop 0
	v_readfirstlane_b32 s14, v1
	s_mul_i32 s13, s13, s14
	s_mul_hi_u32 s13, s14, s13
	s_add_i32 s14, s14, s13
	s_mul_hi_u32 s13, s11, s14
	s_mul_i32 s14, s13, s9
	s_sub_i32 s11, s11, s14
	s_add_i32 s15, s13, 1
	s_sub_i32 s14, s11, s9
	s_cmp_ge_u32 s11, s9
	s_cselect_b32 s13, s15, s13
	s_cselect_b32 s11, s14, s11
	s_add_i32 s14, s13, 1
	s_cmp_ge_u32 s11, s9
	s_cselect_b32 s9, s14, s13
	s_xor_b32 s9, s9, s12
	s_sub_i32 s9, s9, s12
	s_lshl_b32 s11, s9, 2
	s_sub_i32 s12, s3, s11
	s_min_i32 s12, s12, 4
	s_abs_i32 s13, s12
	v_cvt_f32_u32_e32 v1, s13
	s_sub_i32 s15, 0, s13
	s_mul_i32 s9, s9, s8
	s_sub_i32 s8, s10, s9
	v_rcp_iflag_f32_e32 v1, v1
	s_abs_i32 s9, s8
	s_xor_b32 s14, s8, s12
	s_ashr_i32 s14, s14, 31
	v_mul_f32_e32 v1, 0x4f7ffffe, v1
	v_cvt_u32_f32_e32 v1, v1
	s_nop 0
	v_readfirstlane_b32 s16, v1
	s_mul_i32 s15, s15, s16
	s_mul_hi_u32 s15, s16, s15
	s_add_i32 s16, s16, s15
	s_mul_hi_u32 s15, s9, s16
	s_mul_i32 s16, s15, s13
	s_sub_i32 s9, s9, s16
	s_add_i32 s17, s15, 1
	s_sub_i32 s16, s9, s13
	s_cmp_ge_u32 s9, s13
	s_cselect_b32 s15, s17, s15
	s_cselect_b32 s9, s16, s9
	s_add_i32 s16, s15, 1
	s_cmp_ge_u32 s9, s13
	s_cselect_b32 s9, s16, s15
	s_xor_b32 s9, s9, s14
	s_sub_i32 s67, s9, s14
	s_mul_i32 s9, s67, s12
	s_sub_i32 s8, s8, s9
	s_add_i32 s12, s8, s11
	s_load_dwordx4 s[16:19], s[0:1], 0x0
	s_load_dword s11, s[0:1], 0x1c
	s_cbranch_execz .LBB7_8
	s_branch .LBB7_9

.LBB7_11:
	s_mov_b64 s[26:27], 0x80
	s_and_b32 s22, s20, 3
	s_add_i32 m0, s43, 0x18000
	v_lshl_add_u64 v[8:9], v[8:9], 0, s[26:27]
	s_lshl_b32 s48, s21, 6
	s_lshl_b32 s21, s21, 13
	s_lshl_b32 s23, s22, 12
	s_waitcnt vmcnt(4)
	s_barrier
	global_load_lds_dwordx4 v[8:9], off
	v_lshl_add_u64 v[6:7], v[6:7], 0, s[26:27]
	s_add_i32 m0, s43, 0x1a000
	s_add_i32 s49, s43, 0x8000
	s_add_i32 s50, s43, 0xa000
	global_load_lds_dwordx4 v[6:7], off
	v_lshl_add_u64 v[4:5], v[4:5], 0, s[26:27]
	s_mov_b32 m0, s49
	s_add_u32 s0, s30, 0xc080
	global_load_lds_dwordx4 v[4:5], off
	v_lshl_add_u64 v[2:3], v[2:3], 0, s[26:27]
	s_mov_b32 m0, s50
	s_addc_u32 s1, s31, 0
	global_load_lds_dwordx4 v[2:3], off
	s_add_i32 m0, s43, 0x1c000
	v_lshl_add_u64 v[2:3], s[0:1], 0, v[146:147]
	global_load_lds_dwordx4 v[2:3], off
	v_lshl_add_u64 v[2:3], s[0:1], 0, v[150:151]
	s_add_i32 m0, s43, 0x1e000
	s_lshl_b32 s53, s33, 2
	global_load_lds_dwordx4 v[2:3], off
	s_abs_i32 s54, s53
	v_cvt_f32_u32_e32 v6, s54
	v_and_b32_e32 v165, 15, v0
	v_and_b32_e32 v2, 48, v0
	v_lshlrev_b32_e32 v4, 2, v0
	v_rcp_iflag_f32_e32 v6, v6
	v_lshlrev_b32_e32 v5, 6, v0
	v_bfe_u32 v167, v0, 3, 3
	v_and_b32_e32 v0, 7, v0
	s_abs_i32 s57, s33
	v_lshlrev_b32_e32 v168, 4, v0
	v_add_lshl_u32 v169, v0, s10, 4
	v_mul_f32_e32 v0, 0x4f7ffffe, v6
	v_cvt_f32_u32_e32 v6, s57
	s_movk_i32 s0, 0x3c0
	s_mulk_i32 s20, 0x900
	v_cvt_u32_f32_e32 v0, v0
	v_rcp_iflag_f32_e32 v6, v6
	v_and_or_b32 v5, v5, s0, v2
	s_add_i32 s0, s20, 0
	v_lshl_or_b32 v3, v165, 6, v2
	v_and_b32_e32 v4, 32, v4
	s_add_i32 s0, s0, 0x20000
	v_bitop3_b32 v3, v3, s21, v4 bitop3:0xde
	v_bitop3_b32 v166, s23, v5, v4 bitop3:0xf6
	s_movk_i32 s1, 0x90
	v_mov_b32_e32 v4, s0
	v_mad_u32_u24 v5, v165, s1, v4
	v_mad_u32_u24 v4, v167, s1, v4
	v_readfirstlane_b32 s1, v0
	v_mul_f32_e32 v0, 0x4f7ffffe, v6
	v_cvt_u32_f32_e32 v0, v0
	s_sub_i32 s0, 0, s54
	s_mul_i32 s0, s0, s1
	s_mul_hi_u32 s0, s1, s0
	s_add_i32 s59, s1, s0
	s_sub_i32 s0, 0, s57
	v_readfirstlane_b32 s1, v0
	s_waitcnt vmcnt(6)
	s_mul_i32 s0, s0, s1
	v_add_u16_e32 v0, v1, v10
	s_mul_hi_u32 s0, s1, s0
	v_lshrrev_b16_e32 v0, 1, v0
	s_add_i32 s65, 0, 0x10000
	s_add_i32 s66, 0, 0x14000
	s_mov_b32 s23, 0x20000
	s_lshl_b32 s51, s22, 6
	s_waitcnt lgkmcnt(0)
	s_ashr_i32 s52, s11, 31
	s_lshl_b32 s22, s10, 17
	s_and_b32 s21, s9, 0xffff
	s_mov_b32 s20, s8
	s_lshl_b32 s55, s10, 5
	s_mul_i32 s56, s10, 48
	s_bfe_i32 s58, s33, 0x1001c
	s_ashr_i32 s60, s33, 31
	s_add_i32 s61, s1, s0
	s_mul_i32 s62, s10, 0xc0
	s_mul_i32 s63, s10, 0x60
	s_lshl_b32 s64, s10, 4
	v_add_lshl_u32 v152, v11, v0, 1
	v_mov_b32_e32 v153, v147
	v_add_lshl_u32 v154, v12, v0, 1
	v_mov_b32_e32 v155, v147
	v_mov_b64_e32 v[156:157], s[6:7]
	v_add_u32_e32 v170, s65, v166
	v_add_u32_e32 v171, 0, v3
	v_add_u32_e32 v172, s66, v166
	v_add_u32_e32 v173, v5, v2
	v_add_u32_e32 v174, v4, v168
	s_barrier

.LBB7_17:
	s_ashr_i32 s8, s34, 3
	s_add_i32 s34, s68, s8
	s_mov_b64 s[8:9], -1
	s_mov_b64 vcc, s[4:5]
	s_cbranch_vccz .LBB7_19
	s_abs_i32 s9, s34
	s_mul_hi_u32 s35, s9, s59
	s_mul_i32 s68, s35, s54
	s_ashr_i32 s8, s34, 31
	s_sub_i32 s9, s9, s68
	s_xor_b32 s8, s8, s58
	s_add_i32 s68, s35, 1
	s_sub_i32 s69, s9, s54
	s_cmp_ge_u32 s9, s54
	s_cselect_b32 s35, s68, s35
	s_cselect_b32 s9, s69, s9
	s_add_i32 s68, s35, 1
	s_cmp_ge_u32 s9, s54
	s_cselect_b32 s9, s68, s35
	s_xor_b32 s9, s9, s8
	s_sub_i32 s8, s9, s8
	s_lshl_b32 s9, s8, 2
	s_sub_i32 s35, s3, s9
	s_min_i32 s35, s35, 4
	s_abs_i32 s68, s35
	v_cvt_f32_u32_e32 v0, s68
	s_sub_i32 s72, 0, s68
	s_mul_i32 s8, s8, s53
	s_sub_i32 s8, s34, s8
	v_rcp_iflag_f32_e32 v0, v0
	s_abs_i32 s71, s8
	s_xor_b32 s69, s8, s35
	s_ashr_i32 s69, s69, 31
	v_mul_f32_e32 v0, 0x4f7ffffe, v0
	v_cvt_u32_f32_e32 v0, v0
	s_nop 0
	v_readfirstlane_b32 s73, v0
	s_mul_i32 s72, s72, s73
	s_mul_hi_u32 s72, s73, s72
	s_add_i32 s73, s73, s72
	s_mul_hi_u32 s72, s71, s73
	s_mul_i32 s73, s72, s68
	s_sub_i32 s71, s71, s73
	s_add_i32 s73, s72, 1
	s_sub_i32 s74, s71, s68
	s_cmp_ge_u32 s71, s68
	s_cselect_b32 s72, s73, s72
	s_cselect_b32 s71, s74, s71
	s_add_i32 s73, s72, 1
	s_cmp_ge_u32 s71, s68
	s_cselect_b32 s68, s73, s72
	s_xor_b32 s68, s68, s69
	s_sub_i32 s68, s68, s69
	s_mul_i32 s35, s68, s35
	s_sub_i32 s8, s8, s35
	s_add_i32 s35, s8, s9
	s_mov_b64 s[8:9], 0

.LBB9_5:
	s_add_i32 s10, s11, s8
	s_cmpk_gt_i32 s5, 0x4ff
	s_cselect_b64 s[4:5], -1, 0
	s_and_b64 s[4:5], exec, s[4:5]
	s_mov_b64 vcc, s[4:5]
	s_cbranch_vccz .LBB9_7
	s_lshl_b32 s8, s33, 2
	s_abs_i32 s9, s8
	v_cvt_f32_u32_e32 v1, s9
	s_sub_i32 s13, 0, s9
	s_abs_i32 s11, s10
	s_xor_b32 s12, s10, s8
	v_rcp_iflag_f32_e32 v1, v1
	s_ashr_i32 s12, s12, 31
	v_mul_f32_e32 v1, 0x4f7ffffe, v1
	v_cvt_u32_f32_e32 v1, v1
	s_nop 0
	v_readfirstlane_b32 s14, v1
	s_mul_i32 s13, s13, s14
	s_mul_hi_u32 s13, s14, s13
	s_add_i32 s14, s14, s13
	s_mul_hi_u32 s13, s11, s14
	s_mul_i32 s14, s13, s9
	s_sub_i32 s11, s11, s14
	s_add_i32 s15, s13, 1
	s_sub_i32 s14, s11, s9
	s_cmp_ge_u32 s11, s9
	s_cselect_b32 s13, s15, s13
	s_cselect_b32 s11, s14, s11
	s_add_i32 s14, s13, 1
	s_cmp_ge_u32 s11, s9
	s_cselect_b32 s9, s14, s13
	s_xor_b32 s9, s9, s12
	s_sub_i32 s9, s9, s12
	s_lshl_b32 s11, s9, 2
	s_sub_i32 s12, s3, s11
	s_min_i32 s12, s12, 4
	s_abs_i32 s13, s12
	v_cvt_f32_u32_e32 v1, s13
	s_sub_i32 s15, 0, s13
	s_mul_i32 s9, s9, s8
	s_sub_i32 s8, s10, s9
	v_rcp_iflag_f32_e32 v1, v1
	s_abs_i32 s9, s8
	s_xor_b32 s14, s8, s12
	s_ashr_i32 s14, s14, 31
	v_mul_f32_e32 v1, 0x4f7ffffe, v1
	v_cvt_u32_f32_e32 v1, v1
	s_nop 0
	v_readfirstlane_b32 s16, v1
	s_mul_i32 s15, s15, s16
	s_mul_hi_u32 s15, s16, s15
	s_add_i32 s16, s16, s15
	s_mul_hi_u32 s15, s9, s16
	s_mul_i32 s16, s15, s13
	s_sub_i32 s9, s9, s16
	s_add_i32 s17, s15, 1
	s_sub_i32 s16, s9, s13
	s_cmp_ge_u32 s9, s13
	s_cselect_b32 s15, s17, s15
	s_cselect_b32 s9, s16, s9
	s_add_i32 s16, s15, 1
	s_cmp_ge_u32 s9, s13
	s_cselect_b32 s9, s16, s15
	s_xor_b32 s9, s9, s14
	s_sub_i32 s68, s9, s14
	s_mul_i32 s9, s68, s12
	s_sub_i32 s8, s8, s9
	s_add_i32 s12, s8, s11
	s_load_dwordx4 s[16:19], s[0:1], 0x0
	s_load_dword s11, s[0:1], 0x1c
	s_cbranch_execz .LBB9_8
	s_branch .LBB9_9

.LBB9_11:
	s_mov_b64 s[26:27], 0x80
	s_and_b32 s22, s20, 3
	s_add_i32 m0, s43, 0x18000
	v_lshl_add_u64 v[8:9], v[8:9], 0, s[26:27]
	s_lshl_b32 s48, s21, 6
	s_lshl_b32 s21, s21, 13
	s_lshl_b32 s23, s22, 12
	s_waitcnt vmcnt(4)
	s_barrier
	global_load_lds_dwordx4 v[8:9], off
	v_lshl_add_u64 v[6:7], v[6:7], 0, s[26:27]
	s_add_i32 m0, s43, 0x1a000
	s_add_i32 s49, s43, 0x8000
	s_add_i32 s50, s43, 0xa000
	global_load_lds_dwordx4 v[6:7], off
	v_lshl_add_u64 v[4:5], v[4:5], 0, s[26:27]
	s_mov_b32 m0, s49
	s_add_u32 s0, s30, 0xc080
	global_load_lds_dwordx4 v[4:5], off
	v_lshl_add_u64 v[2:3], v[2:3], 0, s[26:27]
	s_mov_b32 m0, s50
	s_addc_u32 s1, s31, 0
	global_load_lds_dwordx4 v[2:3], off
	s_add_i32 m0, s43, 0x1c000
	v_lshl_add_u64 v[2:3], s[0:1], 0, v[146:147]
	global_load_lds_dwordx4 v[2:3], off
	v_lshl_add_u64 v[2:3], s[0:1], 0, v[150:151]
	s_add_i32 m0, s43, 0x1e000
	s_lshl_b32 s53, s33, 2
	global_load_lds_dwordx4 v[2:3], off
	s_abs_i32 s54, s53
	v_cvt_f32_u32_e32 v6, s54
	v_and_b32_e32 v167, 15, v0
	v_and_b32_e32 v2, 48, v0
	v_lshlrev_b32_e32 v4, 2, v0
	v_rcp_iflag_f32_e32 v6, v6
	v_lshlrev_b32_e32 v5, 6, v0
	v_bfe_u32 v169, v0, 3, 3
	v_and_b32_e32 v0, 7, v0
	s_abs_i32 s57, s33
	v_lshlrev_b32_e32 v170, 4, v0
	v_add_lshl_u32 v171, v0, s10, 4
	v_mul_f32_e32 v0, 0x4f7ffffe, v6
	v_cvt_f32_u32_e32 v6, s57
	s_movk_i32 s0, 0x3c0
	s_mulk_i32 s20, 0x900
	v_cvt_u32_f32_e32 v0, v0
	v_rcp_iflag_f32_e32 v6, v6
	v_and_or_b32 v5, v5, s0, v2
	s_add_i32 s0, s20, 0
	v_lshl_or_b32 v3, v167, 6, v2
	v_and_b32_e32 v4, 32, v4
	s_add_i32 s0, s0, 0x20000
	v_bitop3_b32 v3, v3, s21, v4 bitop3:0xde
	v_bitop3_b32 v168, s23, v5, v4 bitop3:0xf6
	s_movk_i32 s1, 0x90
	v_mov_b32_e32 v4, s0
	v_mad_u32_u24 v5, v167, s1, v4
	v_mad_u32_u24 v4, v169, s1, v4
	v_readfirstlane_b32 s1, v0
	v_mul_f32_e32 v0, 0x4f7ffffe, v6
	v_cvt_u32_f32_e32 v0, v0
	s_sub_i32 s0, 0, s54
	s_mul_i32 s0, s0, s1
	s_mul_hi_u32 s0, s1, s0
	s_add_i32 s59, s1, s0
	s_sub_i32 s0, 0, s57
	v_readfirstlane_b32 s1, v0
	s_waitcnt vmcnt(6)
	s_mul_i32 s0, s0, s1
	v_add_u16_e32 v0, v1, v10
	s_mul_hi_u32 s0, s1, s0
	v_lshrrev_b16_e32 v0, 1, v0
	s_add_i32 s65, 0, 0x10000
	s_add_i32 s66, 0, 0x14000
	s_mov_b32 s23, 0x20000
	s_lshl_b32 s51, s22, 6
	s_waitcnt lgkmcnt(0)
	s_ashr_i32 s52, s11, 31
	s_lshl_b32 s22, s10, 17
	s_and_b32 s21, s9, 0xffff
	s_mov_b32 s20, s8
	s_lshl_b32 s55, s10, 5
	s_mul_i32 s56, s10, 48
	s_bfe_i32 s58, s33, 0x1001c
	s_ashr_i32 s60, s33, 31
	s_add_i32 s61, s1, s0
	s_mul_i32 s62, s10, 0xc0
	s_mul_i32 s63, s10, 0x60
	s_lshl_b32 s64, s10, 4
	v_add_lshl_u32 v152, v11, v0, 1
	v_mov_b32_e32 v153, v147
	v_add_lshl_u32 v154, v12, v0, 1
	v_mov_b32_e32 v155, v147
	v_mov_b64_e32 v[156:157], s[6:7]
	v_add_u32_e32 v172, s65, v168
	v_add_u32_e32 v173, 0, v3
	v_add_u32_e32 v174, s66, v168
	v_add_u32_e32 v175, v5, v2
	v_add_u32_e32 v176, v4, v170
	s_barrier

.LBB9_17:
	s_ashr_i32 s8, s34, 3
	s_add_i32 s34, s67, s8
	s_mov_b64 s[8:9], -1
	s_mov_b64 vcc, s[4:5]
	s_cbranch_vccz .LBB9_19
	s_abs_i32 s9, s34
	s_mul_hi_u32 s35, s9, s59
	s_mul_i32 s67, s35, s54
	s_ashr_i32 s8, s34, 31
	s_sub_i32 s9, s9, s67
	s_xor_b32 s8, s8, s58
	s_add_i32 s67, s35, 1
	s_sub_i32 s69, s9, s54
	s_cmp_ge_u32 s9, s54
	s_cselect_b32 s35, s67, s35
	s_cselect_b32 s9, s69, s9
	s_add_i32 s67, s35, 1
	s_cmp_ge_u32 s9, s54
	s_cselect_b32 s9, s67, s35
	s_xor_b32 s9, s9, s8
	s_sub_i32 s8, s9, s8
	s_lshl_b32 s9, s8, 2
	s_sub_i32 s35, s3, s9
	s_min_i32 s35, s35, 4
	s_abs_i32 s67, s35
	v_cvt_f32_u32_e32 v0, s67
	s_sub_i32 s72, 0, s67
	s_mul_i32 s8, s8, s53
	s_sub_i32 s8, s34, s8
	v_rcp_iflag_f32_e32 v0, v0
	s_abs_i32 s71, s8
	s_xor_b32 s69, s8, s35
	s_ashr_i32 s69, s69, 31
	v_mul_f32_e32 v0, 0x4f7ffffe, v0
	v_cvt_u32_f32_e32 v0, v0
	s_nop 0
	v_readfirstlane_b32 s73, v0
	s_mul_i32 s72, s72, s73
	s_mul_hi_u32 s72, s73, s72
	s_add_i32 s73, s73, s72
	s_mul_hi_u32 s72, s71, s73
	s_mul_i32 s73, s72, s67
	s_sub_i32 s71, s71, s73
	s_add_i32 s73, s72, 1
	s_sub_i32 s74, s71, s67
	s_cmp_ge_u32 s71, s67
	s_cselect_b32 s72, s73, s72
	s_cselect_b32 s71, s74, s71
	s_add_i32 s73, s72, 1
	s_cmp_ge_u32 s71, s67
	s_cselect_b32 s67, s73, s72
	s_xor_b32 s67, s67, s69
	s_sub_i32 s67, s67, s69
	s_mul_i32 s35, s67, s35
	s_sub_i32 s8, s8, s35
	s_add_i32 s35, s8, s9
	s_mov_b64 s[8:9], 0
